# speedup vs baseline: 1.0121x; 1.0121x over previous
.Lp_w1t:
	s_sleep 30
	s_load_dwordx2 s[16:17], s[0:1], 0x38
	s_load_dwordx4 s[20:23], s[0:1], 0x48
	v_lshl_or_b32 v2, s2, 8, v0
	v_add_u32_e32 v2, 0xfffec000, v2
	v_mov_b32_e32 v3, 0
	v_mov_b32_e32 v26, v0
	v_lshrrev_b32_e32 v4, 3, v2
	v_lshrrev_b32_e32 v5, 3, v0
	v_lshlrev_b32_e32 v0, 1, v0
	v_and_b32_e32 v4, 0x1fffffe0, v4
	v_and_b32_e32 v6, 0x80, v0
	v_mov_b32_e32 v7, 0
	v_and_or_b32 v4, v5, 20, v4
	s_waitcnt lgkmcnt(0)
	v_lshl_add_u64 v[8:9], s[8:9], 0, v[6:7]
	v_lshlrev_b32_e32 v6, 2, v1
	v_lshl_add_u64 v[0:1], v[8:9], 0, v[6:7]
	v_or_b32_e32 v6, 1, v4
	v_lshlrev_b64 v[10:11], 8, v[6:7]
	v_or_b32_e32 v6, 2, v4
	v_lshlrev_b64 v[12:13], 8, v[6:7]
	v_or_b32_e32 v6, 3, v4
	v_lshlrev_b64 v[14:15], 8, v[6:7]
	v_or_b32_e32 v6, 8, v4
	v_lshlrev_b64 v[16:17], 8, v[6:7]
	v_or_b32_e32 v6, 9, v4
	v_mov_b32_e32 v5, v7
	v_lshlrev_b64 v[18:19], 8, v[6:7]
	v_or_b32_e32 v6, 10, v4
	v_lshlrev_b64 v[8:9], 8, v[4:5]
	v_lshlrev_b64 v[20:21], 8, v[6:7]
	v_or_b32_e32 v6, 11, v4
	v_lshl_add_u64 v[8:9], v[0:1], 0, v[8:9]
	v_lshlrev_b64 v[4:5], 8, v[6:7]
	v_lshl_add_u64 v[10:11], v[0:1], 0, v[10:11]
	v_lshl_add_u64 v[12:13], v[0:1], 0, v[12:13]
	v_lshl_add_u64 v[14:15], v[0:1], 0, v[14:15]
	v_lshl_add_u64 v[16:17], v[0:1], 0, v[16:17]
	v_lshl_add_u64 v[18:19], v[0:1], 0, v[18:19]
	v_lshl_add_u64 v[20:21], v[0:1], 0, v[20:21]
	v_lshl_add_u64 v[0:1], v[0:1], 0, v[4:5]
	global_load_dword v4, v[8:9], off
	global_load_dword v5, v[10:11], off
	global_load_dword v6, v[12:13], off
	global_load_dword v7, v[14:15], off
	global_load_dword v22, v[16:17], off
	global_load_dword v23, v[18:19], off
	global_load_dword v24, v[20:21], off
	global_load_dword v25, v[0:1], off
	v_lshl_add_u64 v[0:1], v[2:3], 4, s[16:17]
	s_sub_u32 s6, s2, 0x140
	s_lshr_b32 s7, s6, 3
	s_and_b32 s6, s6, 7
	s_getpc_b64 s[24:25]
	s_and_b32 s24, s24, 0xfffff000
	v_lshlrev_b32_e32 v32, 7, v26
	v_mov_b32_e32 v33, 0
	s_waitcnt vmcnt(0)
	v_cvt_pk_f16_f32 v4, v4, v5
	v_cvt_pk_f16_f32 v5, v6, v7
	v_cvt_pk_f16_f32 v6, v22, v23
	v_cvt_pk_f16_f32 v7, v24, v25
	global_store_dwordx4 v[0:1], v[4:7], off sc1
	s_cmp_eq_u32 s7, 0
	s_cbranch_scc0 .Lp_q1
	v_lshl_add_u64 v[34:35], s[24:25], 0, v[32:33]
	global_load_dword v31, v[34:35], off sc0 sc1
	s_endpgm
.Lp_q1:
	s_cmp_eq_u32 s7, 1
	s_cbranch_scc0 .Lp_q2
	s_movk_i32 s4, 0x70
	v_cmp_gt_u32_e32 vcc, s4, v26
	s_and_saveexec_b64 s[4:5], vcc
	s_cbranch_execz .Lp_qend
	v_lshl_add_u64 v[34:35], s[24:25], 0, v[32:33]
	v_add_co_u32_e32 v34, vcc, 0x8000, v34
	s_nop 1
	v_addc_co_u32_e32 v35, vcc, 0, v35, vcc
	global_load_dword v8, v[34:35], off sc0 sc1
	s_endpgm
.Lp_q2:
	s_cmp_eq_u32 s7, 2
	s_cbranch_scc0 .Lp_q3
	s_movk_i32 s4, 0xdf
	v_cmp_lt_u32_e32 vcc, s4, v26
	s_and_saveexec_b64 s[4:5], vcc
	s_cbranch_execz .Lp_qend
	s_and_b32 s0, s0, 0xfffff000
	v_lshl_add_u64 v[36:37], s[0:1], 0, v[32:33]
	v_add_co_u32_e32 v36, vcc, 0xffff9000, v36
	s_nop 1
	v_addc_co_u32_e32 v37, vcc, -1, v37, vcc
	global_load_dword v9, v[36:37], off sc0 sc1
	s_endpgm
.Lp_q3:
	v_cmp_gt_u32_e32 vcc, 32, v26
	s_and_saveexec_b64 s[4:5], vcc
	s_cbranch_execz .Lp_qend
	s_cmp_eq_u32 s6, 0
	s_cbranch_scc0 .Lp_q3w
	v_lshl_add_u64 v[10:11], s[20:21], 0, v[32:33]
	global_load_dword v12, v[10:11], off
	s_endpgm
.Lp_q3w:
	s_cmp_eq_u32 s6, 1
	s_cbranch_scc0 .Lp_qend
	v_lshl_add_u64 v[10:11], s[22:23], 0, v[32:33]
	global_load_dword v14, v[10:11], off
